# baseline (speedup 1.0000x reference)
.LBB1_18:
	s_or_b64 exec, exec, s[4:5]
	v_cvt_pk_f16_f32 v41, v40, v41
	v_cvt_pk_f16_f32 v40, v38, v39
	v_cvt_pk_f16_f32 v38, v62, v63
	v_add_u32_e32 v62, 0x8800, v88
	v_cvt_pk_f16_f32 v37, v36, v37
	v_cvt_pk_f16_f32 v36, v34, v35
	v_cvt_pk_f16_f32 v35, v56, v57
	v_cvt_pk_f16_f32 v34, v54, v55
	ds_write2_b64 v62, v[36:37], v[34:35] offset0:8 offset1:12
	v_cvt_pk_f16_f32 v35, v44, v45
	v_cvt_pk_f16_f32 v34, v42, v43
	v_cvt_pk_f16_f32 v37, v48, v49
	v_cvt_pk_f16_f32 v36, v46, v47
	v_cvt_pk_f16_f32 v39, v64, v65
	ds_write2_b64 v62, v[34:35], v[36:37] offset0:16 offset1:20
	v_cvt_pk_f16_f32 v35, v52, v53
	v_cvt_pk_f16_f32 v34, v50, v51
	v_cvt_pk_f16_f32 v37, v60, v61
	v_cvt_pk_f16_f32 v36, v58, v59
	ds_write2_b64 v62, v[40:41], v[38:39] offset1:4
	ds_write2_b64 v62, v[34:35], v[36:37] offset0:24 offset1:28
	ds_read_b128 v[34:37], v89 offset:34816
	v_add_u32_e32 v44, v80, v82
	v_add_u32_e32 v38, 0xffff9e40, v44
	v_ashrrev_i32_e32 v39, 31, v38
	v_lshlrev_b64 v[38:39], 8, v[38:39]
	v_lshl_add_u64 v[42:43], v[70:71], 0, v[38:39]
	ds_read_b128 v[38:41], v90 offset:34816
	s_waitcnt lgkmcnt(1)
	global_store_dwordx4 v[42:43], v[34:37], off nt
	v_cmp_lt_i32_e64 s[4:5], s12, v91
	v_add_u32_e32 v67, 0x5e4, v67
	v_add_u32_e32 v34, 0xffff9e44, v44
	v_ashrrev_i32_e32 v35, 31, v34
	v_lshlrev_b64 v[34:35], 8, v[34:35]
	v_lshl_add_u64 v[34:35], v[70:71], 0, v[34:35]
	s_waitcnt lgkmcnt(0)
	global_store_dwordx4 v[34:35], v[38:41], off nt
	ds_read_b128 v[34:37], v90 offset:35904
	v_add_u32_e32 v82, 0x5e40, v82
	v_add_u32_e32 v38, 0xffff9e48, v44
	v_ashrrev_i32_e32 v39, 31, v38
	v_lshlrev_b64 v[38:39], 8, v[38:39]
	v_lshl_add_u64 v[42:43], v[70:71], 0, v[38:39]
	ds_read_b128 v[38:41], v90 offset:36992
	s_waitcnt lgkmcnt(1)
	global_store_dwordx4 v[42:43], v[34:37], off nt
	s_or_b64 s[10:11], s[4:5], s[10:11]
	s_waitcnt vmcnt(6)
	v_mov_b64_e32 v[42:43], v[26:27]
	v_add_u32_e32 v34, 0xffff9e4c, v44
	v_ashrrev_i32_e32 v35, 31, v34
	v_lshlrev_b64 v[34:35], 8, v[34:35]
	v_lshl_add_u64 v[34:35], v[70:71], 0, v[34:35]
	s_waitcnt lgkmcnt(0)
	global_store_dwordx4 v[34:35], v[38:41], off nt
	s_waitcnt vmcnt(5)
	v_mov_b64_e32 v[36:37], v[32:33]
	v_mov_b64_e32 v[34:35], v[30:31]
	v_mov_b64_e32 v[44:45], v[28:29]
	s_waitcnt vmcnt(4)
	v_mov_b64_e32 v[40:41], v[24:25]
	v_mov_b64_e32 v[38:39], v[22:23]
	v_mov_b64_e32 v[48:49], v[16:17]
	v_mov_b64_e32 v[46:47], v[14:15]
	s_andn2_b64 exec, exec, s[10:11]
	s_cbranch_execz .LBB1_21

.LBB2_18:
	s_or_b64 exec, exec, s[12:13]
	v_cvt_pk_f16_f32 v41, v40, v41
	v_cvt_pk_f16_f32 v40, v38, v39
	v_cvt_pk_f16_f32 v38, v62, v63
	v_add_u32_e32 v62, 0x8800, v88
	v_cvt_pk_f16_f32 v37, v36, v37
	v_cvt_pk_f16_f32 v36, v34, v35
	v_cvt_pk_f16_f32 v35, v56, v57
	v_cvt_pk_f16_f32 v34, v54, v55
	ds_write2_b64 v62, v[36:37], v[34:35] offset0:8 offset1:12
	v_cvt_pk_f16_f32 v35, v48, v49
	v_cvt_pk_f16_f32 v34, v46, v47
	v_cvt_pk_f16_f32 v37, v52, v53
	v_cvt_pk_f16_f32 v36, v50, v51
	v_cvt_pk_f16_f32 v39, v64, v65
	ds_write2_b64 v62, v[34:35], v[36:37] offset0:16 offset1:20
	v_cvt_pk_f16_f32 v35, v44, v45
	v_cvt_pk_f16_f32 v34, v42, v43
	v_cvt_pk_f16_f32 v37, v60, v61
	v_cvt_pk_f16_f32 v36, v58, v59
	ds_write2_b64 v62, v[40:41], v[38:39] offset1:4
	ds_write2_b64 v62, v[34:35], v[36:37] offset0:24 offset1:28
	ds_read_b128 v[34:37], v89 offset:34816
	v_add_u32_e32 v44, v81, v82
	v_add_u32_e32 v38, 0x3a80, v44
	v_ashrrev_i32_e32 v39, 31, v38
	v_lshlrev_b64 v[38:39], 8, v[38:39]
	v_lshl_add_u64 v[42:43], v[70:71], 0, v[38:39]
	ds_read_b128 v[38:41], v90 offset:34816
	s_waitcnt lgkmcnt(1)
	global_store_dwordx4 v[42:43], v[34:37], off nt
	s_and_b64 s[4:5], exec, s[4:5]
	s_or_b64 s[10:11], s[4:5], s[10:11]
	v_add_u32_e32 v34, 0x3a84, v44
	v_ashrrev_i32_e32 v35, 31, v34
	v_lshlrev_b64 v[34:35], 8, v[34:35]
	v_lshl_add_u64 v[34:35], v[70:71], 0, v[34:35]
	s_waitcnt lgkmcnt(0)
	global_store_dwordx4 v[34:35], v[38:41], off nt
	ds_read_b128 v[34:37], v90 offset:35904
	v_add_u32_e32 v82, 0x5e40, v82
	v_add_u32_e32 v38, 0x3a88, v44
	v_ashrrev_i32_e32 v39, 31, v38
	v_lshlrev_b64 v[38:39], 8, v[38:39]
	v_lshl_add_u64 v[42:43], v[70:71], 0, v[38:39]
	ds_read_b128 v[38:41], v90 offset:36992
	s_waitcnt lgkmcnt(1)
	global_store_dwordx4 v[42:43], v[34:37], off nt
	s_nop 1
	v_add_u32_e32 v34, 0x3a8c, v44
	v_ashrrev_i32_e32 v35, 31, v34
	v_lshlrev_b64 v[34:35], 8, v[34:35]
	v_lshl_add_u64 v[34:35], v[70:71], 0, v[34:35]
	s_waitcnt lgkmcnt(0)
	global_store_dwordx4 v[34:35], v[38:41], off nt
	s_waitcnt vmcnt(5)
	v_mov_b64_e32 v[36:37], v[32:33]
	v_mov_b64_e32 v[34:35], v[30:31]
	v_mov_b64_e32 v[32:33], v[24:25]
	v_mov_b64_e32 v[30:31], v[22:23]
	s_waitcnt vmcnt(4)
	v_mov_b64_e32 v[40:41], v[28:29]
	v_mov_b64_e32 v[38:39], v[26:27]
	v_mov_b64_e32 v[28:29], v[16:17]
	v_mov_b64_e32 v[26:27], v[14:15]
	s_andn2_b64 exec, exec, s[10:11]
	s_cbranch_execz .LBB2_21
